# grid barrier: XCD leaders add to TOP without waiting for a return value and poll like everyone else; S5 consumer mid-chunk wait relaxed
# speedup vs baseline: 1.0088x; 1.0004x over previous
; __device__ __forceinline__ unsigned xb_ld(unsigned* p)              { return __hip_atomic_load(p, __ATOMIC_RELAXED, __HIP_MEMORY_SCOPE_AGENT); }
; __device__ __forceinline__ unsigned xb_add(unsigned* p, unsigned v) { return __hip_atomic_fetch_add(p, v, __ATOMIC_RELAXED, __HIP_MEMORY_SCOPE_AGENT); }
; #define XB_SPIN(cond, bar) do { unsigned _sp = 0; while (cond) { __builtin_amdgcn_s_sleep(1); \
;     if ((++_sp & 255u) == 0u) { if (xb_ld(&(bar)[XB_TMO])) break; if (_sp > XB_SPIN_CAP) { atomicAdd(&(bar)[XB_TMO], 1u); break; } } } } while (0)
; __device__ __forceinline__ void xcd_barrier(const XcdBarrier& b) {
;     ...
;         const unsigned old = xb_add(&bar[XB_XSUB(b.x)], 1u);
;         const unsigned gen = old / nloc;
;         if (old + 1u == (gen + 1u) * nloc) {
;             __builtin_amdgcn_fence(__ATOMIC_RELEASE, "agent");
;             asm volatile("s_waitcnt vmcnt(0)" ::: "memory");
;             const unsigned og = xb_add(&bar[XB_TOP], 1u);
;             const unsigned tg = og / nx;
;             if (og + 1u == (tg + 1u) * nx) xb_add(&bar[XB_TOPGEN], 1u);
;             else XB_SPIN(xb_ld(&bar[XB_TOPGEN]) == tg, bar);
.LBB0_54:
	s_andn2_saveexec_b64 s[8:9], s[8:9]
	s_cbranch_execz .LBB0_72
	s_mov_b64 s[8:9], exec
	v_add_u32_e32 v19, 1, v2
	v_mul_lo_u32 v19, v19, v1
	buffer_wbl2 sc1
	s_waitcnt lgkmcnt(0)
	s_waitcnt vmcnt(0)
	v_mbcnt_lo_u32_b32 v2, s8, 0
	v_mbcnt_hi_u32_b32 v2, s9, v2
	v_cmp_eq_u32_e32 vcc, 0, v2
	s_and_saveexec_b64 s[10:11], vcc
	s_cbranch_execz .LBB0_57
	s_bcnt1_i32_b64 s3, s[8:9]
	v_mov_b32_e32 v3, 0x7000
	v_mov_b32_e32 v4, s3
	global_atomic_add v3, v4, s[90:91] offset:1024
.LBB0_57:
	s_or_b64 exec, exec, s[10:11]
	v_cvt_f32_u32_e32 v4, v1
	v_readfirstlane_b32 s3, v3
	s_add_u32 s10, s90, 0x7400
	s_addc_u32 s11, s91, 0
	v_rcp_iflag_f32_e32 v4, v4
	v_add_u32_e32 v2, s3, v2
	v_add_u32_e32 v5, 1, v2
	s_mov_b64 s[12:13], -1
	v_mul_f32_e32 v3, 0x4f7ffffe, v4
	v_cvt_u32_f32_e32 v3, v3
	v_sub_u32_e32 v4, 0, v1
	v_mul_lo_u32 v4, v4, v3
	v_mul_hi_u32 v4, v3, v4
	v_add_u32_e32 v3, v3, v4
	v_mul_hi_u32 v3, v2, v3
	v_mul_lo_u32 v4, v3, v1
	v_sub_u32_e32 v2, v2, v4
	v_add_u32_e32 v6, 1, v3
	v_cmp_ge_u32_e32 vcc, v2, v1
	v_sub_u32_e32 v4, v2, v1
	s_nop 0
	v_cndmask_b32_e32 v3, v3, v6, vcc
	v_cndmask_b32_e32 v2, v2, v4, vcc
	v_add_u32_e32 v4, 1, v3
	v_cmp_ge_u32_e32 vcc, v2, v1
	s_nop 1
	v_cndmask_b32_e32 v4, v3, v4, vcc
	v_mul_lo_u32 v2, v1, v4
	v_add_u32_e32 v1, v2, v1
	v_cmp_eq_u32_e32 vcc, v1, v1
	v_mov_b64_e32 v[2:3], s[10:11]
	s_and_saveexec_b64 s[8:9], vcc
	s_cbranch_execz .LBB0_69
	v_mov_b32_e32 v1, 0
	global_load_dword v2, v1, s[10:11] sc1
	s_mov_b64 s[26:27], 0
	s_waitcnt vmcnt(0)
	v_cmp_lt_u32_e32 vcc, v2, v19
	s_and_saveexec_b64 s[14:15], vcc
	s_cbranch_execz .LBB0_68
	s_add_u32 s12, s90, 0x4200
	s_addc_u32 s13, s91, 0
	s_mov_b32 s3, 1
	s_branch .LBB0_61

; __device__ __forceinline__ unsigned xb_ld(unsigned* p)              { return __hip_atomic_load(p, __ATOMIC_RELAXED, __HIP_MEMORY_SCOPE_AGENT); }
; __device__ __forceinline__ unsigned xb_add(unsigned* p, unsigned v) { return __hip_atomic_fetch_add(p, v, __ATOMIC_RELAXED, __HIP_MEMORY_SCOPE_AGENT); }
; #define XB_SPIN(cond, bar) do { unsigned _sp = 0; while (cond) { __builtin_amdgcn_s_sleep(1); \
;     if ((++_sp & 255u) == 0u) { if (xb_ld(&(bar)[XB_TMO])) break; if (_sp > XB_SPIN_CAP) { atomicAdd(&(bar)[XB_TMO], 1u); break; } } } } while (0)
; __device__ __forceinline__ void xcd_barrier(const XcdBarrier& b) {
;     ...
;         const unsigned old = xb_add(&bar[XB_XSUB(b.x)], 1u);
;         const unsigned gen = old / nloc;
;         if (old + 1u == (gen + 1u) * nloc) {
;             __builtin_amdgcn_fence(__ATOMIC_RELEASE, "agent");
;             asm volatile("s_waitcnt vmcnt(0)" ::: "memory");
;             const unsigned og = xb_add(&bar[XB_TOP], 1u);
;             const unsigned tg = og / nx;
;             if (og + 1u == (tg + 1u) * nx) xb_add(&bar[XB_TOPGEN], 1u);
;             else XB_SPIN(xb_ld(&bar[XB_TOPGEN]) == tg, bar);
.LBB0_182:
	s_andn2_saveexec_b64 s[6:7], s[6:7]
	s_cbranch_execz .LBB0_200
	s_mov_b64 s[6:7], exec
	v_add_u32_e32 v19, 1, v2
	v_mul_lo_u32 v19, v19, v1
	buffer_wbl2 sc1
	s_waitcnt lgkmcnt(0)
	s_waitcnt vmcnt(0)
	v_mbcnt_lo_u32_b32 v2, s6, 0
	v_mbcnt_hi_u32_b32 v2, s7, v2
	v_cmp_eq_u32_e32 vcc, 0, v2
	s_and_saveexec_b64 s[8:9], vcc
	s_cbranch_execz .LBB0_185
	s_bcnt1_i32_b64 s3, s[6:7]
	v_mov_b32_e32 v3, 0x7000
	v_mov_b32_e32 v4, s3
	global_atomic_add v3, v4, s[90:91] offset:1024
.LBB0_185:
	s_or_b64 exec, exec, s[8:9]
	v_cvt_f32_u32_e32 v4, v1
	v_readfirstlane_b32 s3, v3
	s_add_u32 s8, s90, 0x7400
	s_addc_u32 s9, s91, 0
	v_rcp_iflag_f32_e32 v4, v4
	v_add_u32_e32 v2, s3, v2
	v_add_u32_e32 v5, 1, v2
	s_mov_b64 s[10:11], -1
	v_mul_f32_e32 v3, 0x4f7ffffe, v4
	v_cvt_u32_f32_e32 v3, v3
	v_sub_u32_e32 v4, 0, v1
	v_mul_lo_u32 v4, v4, v3
	v_mul_hi_u32 v4, v3, v4
	v_add_u32_e32 v3, v3, v4
	v_mul_hi_u32 v3, v2, v3
	v_mul_lo_u32 v4, v3, v1
	v_sub_u32_e32 v2, v2, v4
	v_add_u32_e32 v6, 1, v3
	v_cmp_ge_u32_e32 vcc, v2, v1
	v_sub_u32_e32 v4, v2, v1
	s_nop 0
	v_cndmask_b32_e32 v3, v3, v6, vcc
	v_cndmask_b32_e32 v2, v2, v4, vcc
	v_add_u32_e32 v4, 1, v3
	v_cmp_ge_u32_e32 vcc, v2, v1
	s_nop 1
	v_cndmask_b32_e32 v4, v3, v4, vcc
	v_mul_lo_u32 v2, v1, v4
	v_add_u32_e32 v1, v2, v1
	v_cmp_eq_u32_e32 vcc, v1, v1
	v_mov_b64_e32 v[2:3], s[8:9]
	s_and_saveexec_b64 s[6:7], vcc
	s_cbranch_execz .LBB0_197
	v_mov_b32_e32 v1, 0
	global_load_dword v2, v1, s[8:9] sc1
	s_mov_b64 s[14:15], 0
	s_waitcnt vmcnt(0)
	v_cmp_lt_u32_e32 vcc, v2, v19
	s_and_saveexec_b64 s[12:13], vcc
	s_cbranch_execz .LBB0_196
	s_add_u32 s10, s90, 0x4200
	s_addc_u32 s11, s91, 0
	s_mov_b32 s3, 1
	s_branch .LBB0_189

; __device__ __forceinline__ unsigned xb_ld(unsigned* p)              { return __hip_atomic_load(p, __ATOMIC_RELAXED, __HIP_MEMORY_SCOPE_AGENT); }
; __device__ __forceinline__ unsigned xb_add(unsigned* p, unsigned v) { return __hip_atomic_fetch_add(p, v, __ATOMIC_RELAXED, __HIP_MEMORY_SCOPE_AGENT); }
; #define XB_SPIN(cond, bar) do { unsigned _sp = 0; while (cond) { __builtin_amdgcn_s_sleep(1); \
;     if ((++_sp & 255u) == 0u) { if (xb_ld(&(bar)[XB_TMO])) break; if (_sp > XB_SPIN_CAP) { atomicAdd(&(bar)[XB_TMO], 1u); break; } } } } while (0)
; __device__ __forceinline__ void xcd_barrier(const XcdBarrier& b) {
;     ...
;         const unsigned old = xb_add(&bar[XB_XSUB(b.x)], 1u);
;         const unsigned gen = old / nloc;
;         if (old + 1u == (gen + 1u) * nloc) {
;             __builtin_amdgcn_fence(__ATOMIC_RELEASE, "agent");
;             asm volatile("s_waitcnt vmcnt(0)" ::: "memory");
;             const unsigned og = xb_add(&bar[XB_TOP], 1u);
;             const unsigned tg = og / nx;
;             if (og + 1u == (tg + 1u) * nx) xb_add(&bar[XB_TOPGEN], 1u);
;             else XB_SPIN(xb_ld(&bar[XB_TOPGEN]) == tg, bar);
.LBB0_1210:
	s_andn2_saveexec_b64 s[10:11], s[10:11]
	s_cbranch_execz .LBB0_1228
	s_mov_b64 s[10:11], exec
	v_add_u32_e32 v19, 1, v2
	v_mul_lo_u32 v19, v19, v1
	buffer_wbl2 sc1
	s_waitcnt lgkmcnt(0)
	s_waitcnt vmcnt(0)
	v_mbcnt_lo_u32_b32 v2, s10, 0
	v_mbcnt_hi_u32_b32 v2, s11, v2
	v_cmp_eq_u32_e32 vcc, 0, v2
	s_and_saveexec_b64 s[12:13], vcc
	s_cbranch_execz .LBB0_1213
	s_bcnt1_i32_b64 s3, s[10:11]
	v_mov_b32_e32 v3, 0x7000
	v_mov_b32_e32 v4, s3
	global_atomic_add v3, v4, s[90:91] offset:1024
.LBB0_1213:
	s_or_b64 exec, exec, s[12:13]
	v_cvt_f32_u32_e32 v4, v1
	v_readfirstlane_b32 s3, v3
	s_add_u32 s12, s90, 0x7400
	s_addc_u32 s13, s91, 0
	v_rcp_iflag_f32_e32 v4, v4
	v_add_u32_e32 v2, s3, v2
	v_add_u32_e32 v5, 1, v2
	s_mov_b64 s[14:15], -1
	v_mul_f32_e32 v3, 0x4f7ffffe, v4
	v_cvt_u32_f32_e32 v3, v3
	v_sub_u32_e32 v4, 0, v1
	v_mul_lo_u32 v4, v4, v3
	v_mul_hi_u32 v4, v3, v4
	v_add_u32_e32 v3, v3, v4
	v_mul_hi_u32 v3, v2, v3
	v_mul_lo_u32 v4, v3, v1
	v_sub_u32_e32 v2, v2, v4
	v_add_u32_e32 v6, 1, v3
	v_cmp_ge_u32_e32 vcc, v2, v1
	v_sub_u32_e32 v4, v2, v1
	s_nop 0
	v_cndmask_b32_e32 v3, v3, v6, vcc
	v_cndmask_b32_e32 v2, v2, v4, vcc
	v_add_u32_e32 v4, 1, v3
	v_cmp_ge_u32_e32 vcc, v2, v1
	s_nop 1
	v_cndmask_b32_e32 v4, v3, v4, vcc
	v_mul_lo_u32 v2, v1, v4
	v_add_u32_e32 v1, v2, v1
	v_cmp_eq_u32_e32 vcc, v1, v1
	v_mov_b64_e32 v[2:3], s[12:13]
	s_and_saveexec_b64 s[10:11], vcc
	s_cbranch_execz .LBB0_1225
	v_mov_b32_e32 v1, 0
	global_load_dword v2, v1, s[12:13] sc1
	s_mov_b64 s[18:19], 0
	s_waitcnt vmcnt(0)
	v_cmp_lt_u32_e32 vcc, v2, v19
	s_and_saveexec_b64 s[16:17], vcc
	s_cbranch_execz .LBB0_1224
	s_add_u32 s14, s90, 0x4200
	s_addc_u32 s15, s91, 0
	s_mov_b32 s3, 1
	s_branch .LBB0_1217

; #define LAS __attribute__((address_space(3)))
; __device__ __forceinline__ unsigned cvt_pk_bf16(float lo, float hi) { unsigned r; asm volatile("v_cvt_pk_bf16_f32 %0, %1, %2" : "=v"(r) : "v"(lo), "v"(hi)); return r; }
; __device__ __forceinline__ float gelu_erf_fast(float v) { return 0.5f * v * (1.0f + erf_as(v * 0.70710678118654752f)); }
; #define LDS_WAIT() asm volatile("s_waitcnt lgkmcnt(0)" ::: "memory")
; __device__ __forceinline__ f32x4 unpack4(u32x2 q) { return (f32x4){bflo(q.x), bfhi(q.x), bflo(q.y), bfhi(q.y)}; }
; __device__ __forceinline__ void phase_s5p(const float* const (&in)[34], unsigned char* ws, LAS unsigned char* lds, int G) {
;     ...
;                 LAS unsigned char* XB = XB0 + (ck & 1) * 4352;
;                 const bf16x8 x0 = *(const LAS bf16x8*)(XB + fr * 272 + 0 * 64 + fq * 16), x1 = *(const LAS bf16x8*)(XB + fr * 272 + 1 * 64 + fq * 16);
;                 const bf16x8 x2 = *(const LAS bf16x8*)(XB + fr * 272 + 2 * 64 + fq * 16), x3 = *(const LAS bf16x8*)(XB + fr * 272 + 3 * 64 + fq * 16);
;                 LDS_WAIT();
;                 *(volatile LAS unsigned*)fcons = (unsigned)(base + ck + 1);
;                 f32x4 ya = __builtin_amdgcn_mfma_f32_16x16x32_bf16(cop[0], x0, (f32x4){0.f, 0.f, 0.f, 0.f}, 0, 0, 0), yb = __builtin_amdgcn_mfma_f32_16x16x32_bf16(cop[1], x1, (f32x4){0.f, 0.f, 0.f, 0.f}, 0, 0, 0);
;                 ya = __builtin_amdgcn_mfma_f32_16x16x32_bf16(cop[2], x2, ya, 0, 0, 0); yb = __builtin_amdgcn_mfma_f32_16x16x32_bf16(cop[3], x3, yb, 0, 0, 0);
;                 const int pos = ck * 16 + fr;
;                 f32x4 yv = (ya + yb) + unpack4(usk) * dsk;
;                 yv[0] = gelu_erf_fast(yv[0]); yv[1] = gelu_erf_fast(yv[1]); yv[2] = gelu_erf_fast(yv[2]); yv[3] = gelu_erf_fast(yv[3]);
;                 if (b == 0 || pos >= NMETA) { u32x2 o; o.x = cvt_pk_bf16(yv[0], yv[1]); o.y = cvt_pk_bf16(yv[2], yv[3]); *(u32x2*)(YS + (size_t)rowof(b, pos) * 2048 + g * 16 + 4 * fq) = o; }
.LBB0_1449:
	s_add_i32 s9, s9, 1
	s_bitcmp1_b32 s8, 0
	s_cselect_b32 s14, 0x1100, 0
	v_add_u32_e32 v44, s14, v83
	ds_read_b128 v[24:27], v44 offset:20992
	ds_read_b128 v[28:31], v44 offset:21056
	ds_read_b128 v[40:43], v44 offset:21120
	ds_read_b128 v[44:47], v44 offset:21184
	s_cmp_eq_u32 s8, 0
	s_waitcnt lgkmcnt(3)
	v_mfma_f32_16x16x32_bf16 v[24:27], v[8:11], v[24:27], 0
	s_waitcnt lgkmcnt(0)
	s_cselect_b64 s[16:17], -1, 0
	s_and_b64 s[16:17], s[4:5], s[16:17]
	s_waitcnt lgkmcnt(2)
	v_mfma_f32_16x16x32_bf16 v[28:31], v[12:15], v[28:31], 0
	v_mov_b32_e32 v48, s18
	s_and_b64 vcc, exec, s[16:17]
	s_waitcnt lgkmcnt(1)
	v_mfma_f32_16x16x32_bf16 v[24:27], v[16:19], v[40:43], v[24:27]
	v_mov_b32_e32 v40, s9
	ds_write_b32 v48, v40 offset:29700
	s_waitcnt lgkmcnt(1)
	v_mfma_f32_16x16x32_bf16 v[28:31], v[20:23], v[44:47], v[28:31]
	s_cbranch_vccnz .LBB0_1446
	s_nop 6
	v_pk_add_f32 v[26:27], v[26:27], v[30:31]
	s_waitcnt vmcnt(2)
	v_lshlrev_b32_e32 v30, 16, v33
	v_and_b32_e32 v31, 0xffff0000, v33
	v_pk_fma_f32 v[26:27], v[6:7], v[30:31], v[26:27]
	v_pk_add_f32 v[24:25], v[24:25], v[28:29]
	v_mul_f32_e32 v30, 0x3f3504f3, v27
	v_fma_f32 v29, |v30|, s30, 1.0
	v_rcp_f32_e32 v31, v29
	v_lshlrev_b32_e32 v28, 16, v32
	v_and_b32_e32 v29, 0xffff0000, v32
	v_pk_fma_f32 v[24:25], v[4:5], v[28:29], v[24:25]
	v_mul_f32_e64 v29, |v30|, s31
	v_fmamk_f32 v28, v31, 0x3f87dc22, v105
	v_mul_f32_e64 v29, |v30|, v29
	v_fmaak_f32 v28, v28, v31, 0x3fb5f0e3
	v_exp_f32_e32 v29, v29
	v_fmaak_f32 v28, v28, v31, 0xbe91a98e
	v_fmaak_f32 v28, v28, v31, 0x3e827906
	v_mul_f32_e64 v28, v28, -v31
	v_fma_f32 v28, v28, v29, 1.0
	v_mul_f32_e32 v29, 0x3f3504f3, v26
	v_bfi_b32 v28, s35, v28, v30
	v_fma_f32 v30, |v29|, s30, 1.0
	v_rcp_f32_e32 v30, v30
	v_mul_f32_e32 v27, 0.5, v27
	v_add_f32_e32 v28, 1.0, v28
	v_mul_f32_e64 v31, |v29|, s31
	v_mul_f32_e32 v27, v27, v28
	v_fmamk_f32 v28, v30, 0x3f87dc22, v105
	v_mul_f32_e64 v31, |v29|, v31
	v_fmaak_f32 v28, v28, v30, 0x3fb5f0e3
	v_exp_f32_e32 v31, v31
	v_fmaak_f32 v28, v28, v30, 0xbe91a98e
	v_fmaak_f32 v28, v28, v30, 0x3e827906
	v_mul_f32_e64 v28, v28, -v30
	v_fma_f32 v28, v28, v31, 1.0
	v_bfi_b32 v28, s35, v28, v29
	v_mul_f32_e32 v29, 0x3f3504f3, v25
	v_fma_f32 v30, |v29|, s30, 1.0
	v_rcp_f32_e32 v30, v30
	v_mul_f32_e32 v26, 0.5, v26
	v_add_f32_e32 v28, 1.0, v28
	v_mul_f32_e64 v31, |v29|, s31
	v_mul_f32_e32 v26, v26, v28
	v_fmamk_f32 v28, v30, 0x3f87dc22, v105
	v_mul_f32_e64 v31, |v29|, v31
	v_fmaak_f32 v28, v28, v30, 0x3fb5f0e3
	v_exp_f32_e32 v31, v31
	v_fmaak_f32 v28, v28, v30, 0xbe91a98e
	v_fmaak_f32 v28, v28, v30, 0x3e827906
	v_mul_f32_e64 v28, v28, -v30
	v_fma_f32 v28, v28, v31, 1.0
	v_bfi_b32 v28, s35, v28, v29
	v_mul_f32_e32 v29, 0x3f3504f3, v24
	v_fma_f32 v30, |v29|, s30, 1.0
	v_rcp_f32_e32 v30, v30
	v_mul_f32_e32 v25, 0.5, v25
	v_add_f32_e32 v28, 1.0, v28
	v_mul_f32_e64 v31, |v29|, s31
	v_mul_f32_e32 v25, v25, v28
	v_fmamk_f32 v28, v30, 0x3f87dc22, v105
	v_mul_f32_e64 v31, |v29|, v31
	v_fmaak_f32 v28, v28, v30, 0x3fb5f0e3
	v_exp_f32_e32 v31, v31
	v_fmaak_f32 v28, v28, v30, 0xbe91a98e
	v_fmaak_f32 v28, v28, v30, 0x3e827906
	v_mul_f32_e64 v28, v28, -v30
	v_fma_f32 v28, v28, v31, 1.0
	v_bfi_b32 v28, s35, v28, v29
	v_mul_f32_e32 v24, 0.5, v24
	v_add_f32_e32 v28, 1.0, v28
	v_mul_f32_e32 v24, v24, v28
	v_lshl_or_b32 v28, s8, 4, v98
	s_cmp_eq_u32 s8, 0
	v_cvt_pk_bf16_f32 v24, v24, v25
	v_cvt_pk_bf16_f32 v25, v26, v27
	v_or_b32_e32 v26, 0x2000, v28
	v_add_u32_e32 v27, s6, v28
	s_cselect_b64 vcc, -1, 0
	v_cndmask_b32_e32 v26, v27, v26, vcc
	v_ashrrev_i32_e32 v27, 31, v26
	v_lshlrev_b64 v[26:27], 12, v[26:27]
	v_lshl_add_u64 v[26:27], v[36:37], 0, v[26:27]
	global_store_dwordx2 v[26:27], v[24:25], off
	s_waitcnt vmcnt(1)
	s_branch .Ls5c_join
